# router: AB-table loads of k-groups 2-4 hoisted next to group 1 (free VGPRs), counted vmcnt waits
# speedup vs baseline: 1.1234x; 1.1234x over previous
; __device__ __forceinline__ void ph_ln_router(const Frame& F, int l, bool dry = false) {
;     ...
;     for (int tile = TILE0 + F.wg; tile < NTILE; tile += F.G) {
;         const int row = tile * 16 + tk; const int s = slot_of_row(tile * 16);
;         const float* ab = (const float*)(F.ws + OFF_AB) + (size_t)(l * 5 + s) * 2048;
;         f32x4 v[4][2];
; #pragma unroll
;         for (int ks = 0; ks < 4; ++ks) { v[ks][0] = vn[ks][0]; v[ks][1] = vn[ks][1]; }
;         if (tile + F.G < NTILE) { const float* xr = F.X + (size_t)((tile + F.G) * 16 + tk) * DM + F.wave * 128 + g * 8;
; #pragma unroll
;             for (int ks = 0; ks < 4; ++ks) { vn[ks][0] = *(const f32x4*)(xr + ks * 32); vn[ks][1] = *(const f32x4*)(xr + ks * 32 + 4); } }
;         float sum = 0.f, sq = 0.f;
; #pragma unroll
;         for (int ks = 0; ks < 4; ++ks)
; #pragma unroll
;             for (int hh = 0; hh < 2; ++hh) { const f32x4 a = v[ks][hh]; sum += (a[0] + a[1]) + (a[2] + a[3]); sq += (a[0] * a[0] + a[1] * a[1]) + (a[2] * a[2] + a[3] * a[3]); }
;         sum = rows_sum(sum); sq = rows_sum(sq);
;         if (g == 0) *(LAS f32x2*)(part + (F.wave * 16 + tk) * 2) = (f32x2){sum, sq};
;         lds_barrier();
;         float ts = 0.f, tq = 0.f;
; #pragma unroll
;         for (int w = 0; w < 8; ++w) { const f32x2 p = *(const LAS f32x2*)(part + (w * 16 + tk) * 2); ts += p.x; tq += p.y; }
;         const float mean = ts * (1.0f / 1024.0f), var = fmaxf(tq * (1.0f / 1024.0f) - mean * mean, 0.f), rstd = rsqrtf(var + 1e-5f);
;         if (F.wave == 0 && g == 0) *(f32x2*)(stats + (size_t)row * 2) = (f32x2){mean, rstd};
;         f32x4 acc[4];
; #pragma unroll
;         for (int et = 0; et < 4; ++et) acc[et] = (f32x4){0.f, 0.f, 0.f, 0.f};
; #pragma unroll
;         for (int ks = 0; ks < 4; ++ks) { const int k = F.wave * 128 + ks * 32 + g * 8;
;             const f32x4 a10 = *(const f32x4*)(ab + k), a11 = *(const f32x4*)(ab + k + 4), b10 = *(const f32x4*)(ab + 1024 + k), b11 = *(const f32x4*)(ab + 1024 + k + 4);
;             const f32x4 h0 = (v[ks][0] - mean) * rstd * a10 + b10, h1 = (v[ks][1] - mean) * rstd * a11 + b11;
;             u32x4 w; w.x = cvt_pk_bf16(h0[0], h0[1]); w.y = cvt_pk_bf16(h0[2], h0[3]); w.z = cvt_pk_bf16(h1[0], h1[1]); w.w = cvt_pk_bf16(h1[2], h1[3]);
;             *(u32x4*)(F.HB + (size_t)row * DM + k) = w;
;             bf16x8 af; __builtin_memcpy(&af, &w, 16);
; #pragma unroll
.LBB0_1320:
	s_or_b64 exec, exec, s[8:9]
	v_readlane_b32 s8, v254, 0
	s_add_i32 s8, s8, s13
	s_lshr_b32 s8, s8, 13
	s_cmp_gt_i32 s2, 63
	s_cselect_b32 s2, s8, 4
	v_readlane_b32 s8, v255, 2
	s_mul_i32 s8, s8, 5
	v_readlane_b32 s9, v255, 3
	s_add_i32 s64, s2, s8
	s_lshl_b64 s[8:9], s[64:65], 13
	v_readlane_b32 s2, v252, 18
	s_add_u32 s54, s2, s8
	v_readlane_b32 s2, v252, 19
	s_addc_u32 s55, s2, s9
	s_add_u32 s8, s54, 0x1000
	s_addc_u32 s9, s55, 0
	v_lshlrev_b64 v[190:191], 2, v[136:137]
	v_lshl_add_u64 v[170:171], s[54:55], 0, v[190:191]
	v_lshl_add_u64 v[194:195], s[8:9], 0, v[190:191]
	global_load_dwordx4 v[166:169], v[170:171], off offset:16
	s_nop 0
	global_load_dwordx4 v[170:173], v[170:171], off
	s_nop 0
	global_load_dwordx4 v[190:193], v[194:195], off offset:16
	s_nop 0
	global_load_dwordx4 v[194:197], v[194:195], off
	v_lshlrev_b64 v[246:247], 2, v[138:139]
	v_lshl_add_u64 v[248:249], s[8:9], 0, v[246:247]
	v_lshl_add_u64 v[246:247], s[54:55], 0, v[246:247]
	global_load_dwordx4 v[210:213], v[246:247], off offset:16
	global_load_dwordx4 v[198:201], v[246:247], off
	global_load_dwordx4 v[202:205], v[248:249], off offset:16
	global_load_dwordx4 v[206:209], v[248:249], off
	v_lshlrev_b64 v[246:247], 2, v[140:141]
	v_lshl_add_u64 v[248:249], s[8:9], 0, v[246:247]
	v_lshl_add_u64 v[246:247], s[54:55], 0, v[246:247]
	global_load_dwordx4 v[214:217], v[246:247], off offset:16
	global_load_dwordx4 v[218:221], v[246:247], off
	global_load_dwordx4 v[222:225], v[248:249], off offset:16
	global_load_dwordx4 v[226:229], v[248:249], off
	v_lshlrev_b64 v[246:247], 2, v[142:143]
	v_lshl_add_u64 v[248:249], s[8:9], 0, v[246:247]
	v_lshl_add_u64 v[246:247], s[54:55], 0, v[246:247]
	global_load_dwordx4 v[230:233], v[246:247], off offset:16
	global_load_dwordx4 v[234:237], v[246:247], off
	global_load_dwordx4 v[238:241], v[248:249], off offset:16
	global_load_dwordx4 v[242:245], v[248:249], off
	v_sub_f32_e32 v129, v129, v148
	v_sub_f32_e32 v128, v128, v148
	v_sub_f32_e32 v125, v125, v148
	v_sub_f32_e32 v124, v124, v148
	v_sub_f32_e32 v131, v131, v148
	v_sub_f32_e32 v130, v130, v148
	v_pk_mul_f32 v[128:129], v[128:129], v[150:151] op_sel_hi:[1,0]
	v_sub_f32_e32 v127, v127, v148
	v_sub_f32_e32 v126, v126, v148
	v_pk_mul_f32 v[124:125], v[124:125], v[150:151] op_sel_hi:[1,0]
	v_lshlrev_b64 v[152:153], 11, v[152:153]
	v_pk_mul_f32 v[130:131], v[130:131], v[150:151] op_sel_hi:[1,0]
	v_pk_mul_f32 v[126:127], v[126:127], v[150:151] op_sel_hi:[1,0]
	v_sub_f32_e32 v121, v121, v148
	v_sub_f32_e32 v120, v120, v148
	v_sub_f32_e32 v119, v119, v148
	v_sub_f32_e32 v118, v118, v148
	v_sub_f32_e32 v117, v117, v148
	v_sub_f32_e32 v116, v116, v148
	v_sub_f32_e32 v123, v123, v148
	v_sub_f32_e32 v122, v122, v148
	v_pk_mul_f32 v[120:121], v[120:121], v[150:151] op_sel_hi:[1,0]
	v_pk_mul_f32 v[116:117], v[116:117], v[150:151] op_sel_hi:[1,0]
	v_pk_mul_f32 v[118:119], v[118:119], v[150:151] op_sel_hi:[1,0]
	v_pk_mul_f32 v[122:123], v[122:123], v[150:151] op_sel_hi:[1,0]
	v_sub_f32_e32 v113, v113, v148
	v_sub_f32_e32 v112, v112, v148
	v_pk_mul_f32 v[112:113], v[112:113], v[150:151] op_sel_hi:[1,0]
	v_sub_f32_e32 v111, v111, v148
	v_sub_f32_e32 v110, v110, v148
	v_sub_f32_e32 v109, v109, v148
	v_sub_f32_e32 v108, v108, v148
	v_sub_f32_e32 v115, v115, v148
	v_sub_f32_e32 v114, v114, v148
	v_pk_mul_f32 v[108:109], v[108:109], v[150:151] op_sel_hi:[1,0]
	v_pk_mul_f32 v[110:111], v[110:111], v[150:151] op_sel_hi:[1,0]
	v_pk_mul_f32 v[114:115], v[114:115], v[150:151] op_sel_hi:[1,0]
	v_sub_f32_e32 v105, v105, v148
	v_sub_f32_e32 v104, v104, v148
	v_sub_f32_e32 v107, v107, v148
	v_sub_f32_e32 v106, v106, v148
	v_pk_mul_f32 v[104:105], v[104:105], v[150:151] op_sel_hi:[1,0]
	v_sub_f32_e32 v103, v103, v148
	v_sub_f32_e32 v102, v102, v148
	v_sub_f32_e32 v101, v101, v148
	v_sub_f32_e32 v100, v100, v148
	v_pk_mul_f32 v[106:107], v[106:107], v[150:151] op_sel_hi:[1,0]
	v_pk_mul_f32 v[100:101], v[100:101], v[150:151] op_sel_hi:[1,0]
	v_pk_mul_f32 v[102:103], v[102:103], v[150:151] op_sel_hi:[1,0]
	s_mov_b32 s2, 0xf149f2ca
	s_mov_b64 s[30:31], -1
	s_waitcnt vmcnt(13)
	v_pk_fma_f32 v[124:125], v[124:125], v[166:167], v[190:191]
	s_waitcnt vmcnt(12)
	v_pk_fma_f32 v[128:129], v[128:129], v[170:171], v[194:195]
	v_pk_fma_f32 v[130:131], v[130:131], v[172:173], v[196:197]
	v_pk_fma_f32 v[168:169], v[126:127], v[168:169], v[192:193]
	v_cvt_pk_bf16_f32 v126, v128, v129
	v_cvt_pk_bf16_f32 v127, v130, v131
	v_cvt_pk_bf16_f32 v128, v124, v125
	v_lshl_add_u64 v[124:125], s[76:77], 0, v[152:153]
	v_lshl_add_u64 v[130:131], v[136:137], 1, v[124:125]
	v_cvt_pk_bf16_f32 v129, v168, v169
	global_store_dwordx4 v[130:131], v[126:129], off
	v_mfma_f32_16x16x32_bf16 v[166:169], v[126:129], v[12:15], 0
	s_waitcnt vmcnt(10)
	v_pk_fma_f32 v[130:131], v[118:119], v[212:213], v[204:205]
	v_mfma_f32_16x16x32_bf16 v[170:173], v[126:129], v[20:23], 0
	s_waitcnt vmcnt(9)
	v_pk_fma_f32 v[120:121], v[120:121], v[198:199], v[206:207]
	v_pk_fma_f32 v[118:119], v[116:117], v[210:211], v[202:203]
	v_pk_fma_f32 v[122:123], v[122:123], v[200:201], v[208:209]
	v_mfma_f32_16x16x32_bf16 v[190:193], v[126:129], v[36:39], 0
	v_cvt_pk_bf16_f32 v116, v120, v121
	v_cvt_pk_bf16_f32 v117, v122, v123
	v_cvt_pk_bf16_f32 v118, v118, v119
	v_mfma_f32_16x16x32_bf16 v[126:129], v[126:129], v[52:55], 0
	v_cvt_pk_bf16_f32 v119, v130, v131
	v_lshl_add_u64 v[120:121], v[138:139], 1, v[124:125]
	global_store_dwordx4 v[120:121], v[116:119], off
	v_mfma_f32_16x16x32_bf16 v[120:123], v[116:119], v[4:7], v[166:169]
	v_mfma_f32_16x16x32_bf16 v[166:169], v[116:119], v[24:27], v[170:173]
	v_mfma_f32_16x16x32_bf16 v[170:173], v[116:119], v[40:43], v[190:193]
	v_mfma_f32_16x16x32_bf16 v[116:119], v[116:119], v[56:59], v[126:129]
	s_nop 2
	s_mov_b64 s[8:9], -1
	s_waitcnt vmcnt(7)
; __device__ __forceinline__ void lds_barrier() { asm volatile("s_waitcnt lgkmcnt(0)\n\ts_barrier" ::: "memory"); }
; __device__ __forceinline__ unsigned cvt_pk_bf16(float lo, float hi) { unsigned r; asm volatile("v_cvt_pk_bf16_f32 %0, %1, %2" : "=v"(r) : "v"(lo), "v"(hi)); return r; }
; __device__ __forceinline__ void ph_ln_router(const Frame& F, int l, bool dry = false) {
;     ...
;         for (int ks = 0; ks < 4; ++ks) { const int k = F.wave * 128 + ks * 32 + g * 8;
;             const f32x4 a10 = *(const f32x4*)(ab + k), a11 = *(const f32x4*)(ab + k + 4), b10 = *(const f32x4*)(ab + 1024 + k), b11 = *(const f32x4*)(ab + 1024 + k + 4);
;             const f32x4 h0 = (v[ks][0] - mean) * rstd * a10 + b10, h1 = (v[ks][1] - mean) * rstd * a11 + b11;
;             u32x4 w; w.x = cvt_pk_bf16(h0[0], h0[1]); w.y = cvt_pk_bf16(h0[2], h0[3]); w.z = cvt_pk_bf16(h1[0], h1[1]); w.w = cvt_pk_bf16(h1[2], h1[3]);
;             *(u32x4*)(F.HB + (size_t)row * DM + k) = w;
;             bf16x8 af; __builtin_memcpy(&af, &w, 16);
; #pragma unroll
;             for (int et = 0; et < 4; ++et) acc[et] = __builtin_amdgcn_mfma_f32_16x16x32_bf16(af, rwf[et][ks], acc[et], 0, 0, 0);
;         }
; #pragma unroll
;         for (int et = 0; et < 4; ++et)
; #pragma unroll
;             for (int i = 0; i < 4; ++i) LP[(F.wave * 16 + 4 * g + i) * 64 + et * 16 + tk] = acc[et][i];
;         lds_barrier();
;         {
;             const int t = 2 * F.wave + (g & 1), r2 = tile * 16 + t;
;             float sc[4], key[4];
; #pragma unroll
;             for (int q = 0; q < 4; ++q) { float lgt = 0.f;
; #pragma unroll
;                 for (int w = 0; w < 8; ++w) lgt += LP[(w * 16 + t) * 64 + tk + 16 * q];
;                 sc[q] = sigmoidf_(lgt); key[q] = sc[q] + rb[q]; }
;             unsigned taken = 0u; int se[6]; float ss[6]; float tot = 0.f;
; #pragma unroll
;             for (int sel = 0; sel < 6; ++sel) {
;                 float bk = -1e30f, bs = 0.f; int be = 0;
; #pragma unroll
;                 for (int q = 0; q < 4; ++q) if (!((taken >> q) & 1u) && key[q] > bk) { bk = key[q]; be = tk + 16 * q; bs = sc[q]; }
;                 topk_step<0xB1>(bk, be, bs); topk_step<0x4E>(bk, be, bs); topk_step<0x141>(bk, be, bs); topk_step<0x140>(bk, be, bs);
;                 if ((be & 15) == tk) taken |= 1u << (be >> 4);
;                 se[sel] = be; ss[sel] = bs; tot += bs;
	v_pk_fma_f32 v[128:129], v[110:111], v[216:217], v[224:225]
	s_waitcnt vmcnt(6)
	v_pk_fma_f32 v[112:113], v[112:113], v[218:219], v[226:227]
	v_pk_fma_f32 v[110:111], v[108:109], v[214:215], v[222:223]
	v_cvt_pk_bf16_f32 v108, v112, v113
	v_lshl_add_u64 v[112:113], v[140:141], 1, v[124:125]
	v_pk_fma_f32 v[114:115], v[114:115], v[220:221], v[228:229]
	s_nop 0
	v_cvt_pk_bf16_f32 v109, v114, v115
	v_cvt_pk_bf16_f32 v110, v110, v111
	v_cvt_pk_bf16_f32 v111, v128, v129
	global_store_dwordx4 v[112:113], v[108:111], off
	v_mfma_f32_16x16x32_bf16 v[112:115], v[108:111], v[8:11], v[120:123]
	v_mfma_f32_16x16x32_bf16 v[120:123], v[108:111], v[28:31], v[166:169]
	v_mfma_f32_16x16x32_bf16 v[126:129], v[108:111], v[44:47], v[170:173]
	v_mfma_f32_16x16x32_bf16 v[108:111], v[108:111], v[60:63], v[116:119]
	s_nop 2
	s_waitcnt vmcnt(4)
	v_pk_fma_f32 v[118:119], v[102:103], v[232:233], v[240:241]
	s_waitcnt vmcnt(3)
	v_pk_fma_f32 v[104:105], v[104:105], v[234:235], v[242:243]
	v_pk_fma_f32 v[106:107], v[106:107], v[236:237], v[244:245]
	v_pk_fma_f32 v[102:103], v[100:101], v[230:231], v[238:239]
	v_cvt_pk_bf16_f32 v100, v104, v105
	v_lshl_add_u64 v[104:105], v[142:143], 1, v[124:125]
	v_cvt_pk_bf16_f32 v101, v106, v107
	v_cvt_pk_bf16_f32 v102, v102, v103
	v_cvt_pk_bf16_f32 v103, v118, v119
	global_store_dwordx4 v[104:105], v[100:103], off
	v_mfma_f32_16x16x32_bf16 v[104:107], v[100:103], v[16:19], v[112:115]
	v_add_u32_e32 v124, 0x8000, v164
	v_mfma_f32_16x16x32_bf16 v[112:115], v[100:103], v[32:35], v[120:123]
	v_mfma_f32_16x16x32_bf16 v[116:119], v[100:103], v[48:51], v[126:129]
	s_nop 1
	v_add_u32_e32 v120, 0x4000, v164
	v_add_u32_e32 v121, 0x5000, v164
	v_add_u32_e32 v122, 0x6000, v164
	v_mfma_f32_16x16x32_bf16 v[100:103], v[100:103], v[64:67], v[108:111]
	v_add_u32_e32 v123, 0x7000, v164
	s_nop 1
	v_add_u32_e32 v108, 0x1000, v163
	ds_write2_b32 v108, v104, v112 offset1:16
	ds_write2_b32 v108, v105, v113 offset0:64 offset1:80
	ds_write2_b32 v108, v106, v114 offset0:128 offset1:144
	ds_write2_b32 v108, v107, v115 offset0:192 offset1:208
	ds_write2_b32 v108, v116, v100 offset0:32 offset1:48
	ds_write2_b32 v108, v117, v101 offset0:96 offset1:112
	ds_write2_b32 v108, v118, v102 offset0:160 offset1:176
	ds_write2_b32 v108, v119, v103 offset0:224 offset1:240
	s_waitcnt lgkmcnt(0)
	s_barrier
	v_add_u32_e32 v118, 0x1000, v164
	ds_read2_b32 v[102:103], v118 offset1:16
	v_add_u32_e32 v119, 0x2000, v164
	ds_read2_b32 v[104:105], v119 offset1:16
	ds_read2_b32 v[108:109], v120 offset1:16
	ds_read2_b32 v[110:111], v121 offset1:16
	s_waitcnt lgkmcnt(3)
	v_add_f32_e32 v100, 0, v102
	ds_read2_b32 v[112:113], v122 offset1:16
	s_waitcnt lgkmcnt(3)
	v_add_f32_e32 v100, v100, v104
	v_add_u32_e32 v104, 0x3000, v164
	ds_read2_b32 v[106:107], v104 offset1:16
	v_add_f32_e32 v102, 0, v103
	ds_read2_b32 v[114:115], v123 offset1:16
	v_add_f32_e32 v102, v102, v105
	ds_read2_b32 v[116:117], v124 offset1:16
	s_waitcnt lgkmcnt(2)
	v_add_f32_e32 v100, v100, v106
	v_add_f32_e32 v102, v102, v107
	ds_read2_b32 v[106:107], v118 offset0:32 offset1:48
	v_add_f32_e32 v100, v100, v108
	v_add_f32_e32 v102, v102, v109
	ds_read2_b32 v[108:109], v119 offset0:32 offset1:48
	v_add_f32_e32 v100, v100, v110
	v_add_f32_e32 v102, v102, v111
	ds_read2_b32 v[110:111], v104 offset0:32 offset1:48
	v_add_f32_e32 v100, v100, v112
	v_add_f32_e32 v102, v102, v113
	ds_read2_b32 v[112:113], v120 offset0:32 offset1:48
	s_waitcnt lgkmcnt(5)
	v_add_f32_e32 v100, v100, v114
	v_add_f32_e32 v102, v102, v115
	ds_read2_b32 v[114:115], v121 offset0:32 offset1:48
	s_waitcnt lgkmcnt(5)
	v_add_f32_e32 v100, v100, v116
	v_add_f32_e32 v102, v102, v117
	s_waitcnt lgkmcnt(4)
	v_add_f32_e32 v105, 0, v106
	ds_read2_b32 v[116:117], v122 offset0:32 offset1:48
	s_waitcnt lgkmcnt(4)
	v_add_f32_e32 v105, v105, v108
	ds_read2_b32 v[118:119], v123 offset0:32 offset1:48
	s_waitcnt lgkmcnt(4)
	v_add_f32_e32 v104, v105, v110
	ds_read2_b32 v[120:121], v124 offset0:32 offset1:48
	v_add_f32_e32 v106, 0, v107
	s_waitcnt lgkmcnt(4)
	v_add_f32_e32 v104, v104, v112
	v_add_f32_e32 v106, v106, v109
	v_mul_f32_e32 v100, 0xbfb8aa3b, v100
	s_waitcnt lgkmcnt(3)
	v_add_f32_e32 v104, v104, v114
	v_add_f32_e32 v106, v106, v111
	v_exp_f32_e32 v100, v100
	s_waitcnt lgkmcnt(2)
	v_add_f32_e32 v104, v104, v116
	v_add_f32_e32 v106, v106, v113
	v_mul_f32_e32 v102, 0xbfb8aa3b, v102
	s_waitcnt lgkmcnt(1)
	v_add_f32_e32 v104, v104, v118
	v_add_f32_e32 v106, v106, v115
	v_exp_f32_e32 v102, v102
	s_waitcnt lgkmcnt(0)
	v_add_f32_e32 v104, v104, v120
	v_add_f32_e32 v106, v106, v117
	v_mul_f32_e32 v104, 0xbfb8aa3b, v104
	v_add_f32_e32 v106, v106, v119
	v_add_f32_e32 v100, 1.0, v100
	v_exp_f32_e32 v104, v104
	v_add_f32_e32 v106, v106, v121
	v_rcp_f32_e32 v100, v100
	v_mul_f32_e32 v106, 0xbfb8aa3b, v106
	v_add_f32_e32 v102, 1.0, v102
	v_exp_f32_e32 v106, v106
	v_rcp_f32_e32 v102, v102
	v_add_f32_e32 v104, 1.0, v104
	v_add_f32_e32 v101, v133, v100
	v_rcp_f32_e32 v104, v104
	v_add_f32_e32 v106, 1.0, v106
	v_cmp_lt_f32_e32 vcc, s2, v101
	v_add_f32_e32 v103, v145, v102
	v_rcp_f32_e32 v106, v106
	v_cndmask_b32_e32 v108, v188, v101, vcc
	v_cmp_gt_f32_e64 s[54:55], v103, v108
	v_add_f32_e32 v105, v154, v104
	v_cndmask_b32_e32 v109, 0, v100, vcc
	v_cndmask_b32_e32 v110, 0, v1, vcc
	v_cndmask_b32_e64 v108, v108, v103, s[54:55]
	v_cndmask_b32_e64 v109, v109, v102, s[54:55]
	v_cndmask_b32_e64 v110, v110, v156, s[54:55]
	v_cmp_gt_f32_e64 s[54:55], v105, v108
	v_add_f32_e32 v107, v155, v106
	s_nop 0
	v_cndmask_b32_e64 v108, v108, v105, s[54:55]
	v_cndmask_b32_e64 v111, v109, v104, s[54:55]
	v_cndmask_b32_e64 v110, v110, v157, s[54:55]
	v_cmp_gt_f32_e64 s[54:55], v107, v108
	s_nop 1
	v_cndmask_b32_e64 v109, v108, v107, s[54:55]
	v_cndmask_b32_e64 v108, v111, v106, s[54:55]
	v_cndmask_b32_e64 v110, v110, v158, s[54:55]
	v_mov_b32_e32 v111, v109
	v_mov_b32_e32 v112, v108
	v_mov_b32_e32 v113, v110
	v_mov_b32_dpp v111, v111 quad_perm:[1,0,3,2] row_mask:0xf bank_mask:0xf
	v_mov_b32_dpp v112, v112 quad_perm:[1,0,3,2] row_mask:0xf bank_mask:0xf
	v_mov_b32_dpp v113, v113 quad_perm:[1,0,3,2] row_mask:0xf bank_mask:0xf
	v_cmp_nlt_f32_e64 s[54:55], v109, v111
	s_and_saveexec_b64 s[24:25], s[54:55]
	s_cbranch_execz .LBB0_1324
	v_cmp_eq_f32_e64 s[54:55], v109, v111
	s_mov_b64 s[30:31], 0
	s_and_saveexec_b64 s[56:57], s[54:55]
	v_cmp_lt_i32_e64 s[54:55], v113, v110
	s_and_b64 s[30:31], s[54:55], exec
	s_or_b64 exec, exec, s[56:57]
	s_orn2_b64 s[30:31], s[30:31], exec
